# MoBA loops: wave halves staggered by half a step (second barrier mid-softmax, next-tile DMA issued at the shared barrier instance)
# baseline (speedup 1.0000x reference)
; __device__ __forceinline__ void moba_unit(const MobaArgs& A, int b, int h, int qb, LAS unsigned char* lds, int wave, bool tables) {
;     ...
;     float mref = 0.f, l = 0.f; f32x16 o[2], cn;
;     float zf = 0.f; asm volatile("" : "+v"(zf));
; #pragma unroll
;     for (int r = 0; r < 16; ++r) { o[0][r] = zf; o[1][r] = zf; cn[r] = zf; }
;     const int NP = 2 * (qb + 1); const int qmin = q0 + 32 * wid;
;     const float bfar = lut[LUTA_TOP - 1000];
;     stage_tile<64>(lds + L_BUF + 16384, Kh + (size_t)(q0 + 64) * 512, Vh + (size_t)(q0 + 64) * 512, 512, 512, wid, lane);
.LBB0_643:
	v_and_b32_e32 v4, 0x4000, v0
	v_cmp_gt_f32_e32 vcc, v54, v3
	s_and_b32 s3, s30, 0x3fffffc0
	s_lshl_b32 s3, s3, 2
	v_cndmask_b32_e64 v3, 0, 1, vcc
	v_cmp_eq_u32_e32 vcc, 0, v4
	s_add_i32 s3, s3, 0
	s_lshl_b32 s95, s81, 1
	v_cndmask_b32_e64 v4, 0, 1, vcc
	s_and_b64 vcc, vcc, s[16:17]
	v_cndmask_b32_e32 v3, v4, v3, vcc
	v_and_b32_e32 v3, 1, v3
	v_cmp_eq_u32_e32 vcc, 1, v3
	s_add_i32 s3, s3, 0x13000
	s_and_b64 vcc, s[22:23], vcc
	s_add_i32 s95, s95, 2
	s_bitset1_b32 s31, 16
	s_add_u32 s4, s72, s31
	v_lshlrev_b32_e32 v1, 9, v131
	s_addc_u32 s5, s73, 0
	v_lshlrev_b32_e64 v8, v2, 1
	s_add_u32 s6, s74, s31
	v_lshlrev_b32_e32 v2, 1, v1
	v_mov_b32_e32 v3, v113
	s_addc_u32 s7, s75, 0
	v_lshl_add_u64 v[4:5], s[4:5], 0, v[2:3]
	s_lshl_b64 s[4:5], s[18:19], 1
	v_lshlrev_b32_e32 v6, 9, v32
	v_mov_b32_e32 v32, v113
	v_lshl_add_u64 v[4:5], v[4:5], 0, s[4:5]
	s_add_i32 m0, s82, 0x4000
	v_mov_b32_e32 v1, 0x4000
	global_load_lds_dwordx4 v[4:5], off
	v_lshlrev_b32_e32 v4, 1, v6
	v_mov_b32_e32 v5, v113
	v_lshl_add_u64 v[6:7], s[6:7], 0, v[4:5]
	s_lshl_b64 s[6:7], s[20:21], 1
	v_lshl_add_u64 v[6:7], v[6:7], 0, s[6:7]
	v_lshl_add_u64 v[6:7], v[6:7], 0, v[112:113]
	s_add_i32 m0, s82, 0x6000
	v_cndmask_b32_e32 v1, v8, v1, vcc
	global_load_lds_dwordx4 v[6:7], off
	v_readlane_b32 s8, v254, 12
	v_or_b32_e32 v133, v1, v0
	v_mov_b32_e32 v33, v32
	v_mov_b32_e32 v0, s8
	ds_read_b32 v135, v0
	v_lshl_add_u64 v[0:1], s[72:73], 0, v[2:3]
	v_lshl_add_u64 v[136:137], v[0:1], 0, s[4:5]
	v_lshl_add_u64 v[0:1], s[74:75], 0, v[4:5]
	v_lshl_add_u64 v[0:1], v[0:1], 0, s[6:7]
	v_lshl_add_u64 v[138:139], v[0:1], 0, v[112:113]
	v_lshlrev_b32_e32 v0, 4, v131
	v_and_b32_e32 v163, 0xc0, v0
	v_lshlrev_b32_e32 v0, 1, v131
	v_mov_b32_e32 v34, v32
	v_mov_b32_e32 v35, v32
	v_mov_b32_e32 v36, v32
	v_mov_b32_e32 v37, v32
	v_mov_b32_e32 v38, v32
	v_mov_b32_e32 v39, v32
	v_mov_b32_e32 v40, v32
	v_mov_b32_e32 v41, v32
	v_mov_b32_e32 v42, v32
	v_mov_b32_e32 v43, v32
	v_mov_b32_e32 v44, v32
	v_mov_b32_e32 v45, v32
	v_mov_b32_e32 v46, v32
	v_mov_b32_e32 v47, v32
	v_and_b32_e32 v165, 32, v0
	v_readlane_b32 s6, v254, 13
	s_lshl_b32 s71, s89, 1
	v_mov_b64_e32 v[16:17], v[32:33]
	v_mov_b64_e32 v[0:1], v[32:33]
	s_mov_b32 s87, 0
	s_or_b32 s86, s92, 0x80
	s_or_b32 s62, s96, 31
	v_lshlrev_b32_e32 v158, 10, v156
	v_lshlrev_b32_e32 v159, 4, v155
	v_lshlrev_b32_e32 v160, 2, v156
	v_cmp_gt_u32_e64 s[4:5], 32, v131
	v_lshl_add_u32 v112, v155, 2, s3
	v_lshlrev_b32_e32 v161, 8, v156
	v_add_u32_e32 v166, s6, v132
	s_or_b32 s63, s71, 0xffffffe0
	v_mov_b32_e32 v162, 0
	s_mov_b32 s84, -2
	s_mov_b32 s97, 0
	v_mov_b64_e32 v[18:19], v[34:35]
	v_mov_b64_e32 v[20:21], v[36:37]
	v_mov_b64_e32 v[22:23], v[38:39]
	v_mov_b64_e32 v[24:25], v[40:41]
	v_mov_b64_e32 v[26:27], v[42:43]
	v_mov_b64_e32 v[28:29], v[44:45]
	v_mov_b64_e32 v[30:31], v[46:47]
	v_mov_b64_e32 v[2:3], v[34:35]
	v_mov_b64_e32 v[4:5], v[36:37]
	v_mov_b64_e32 v[6:7], v[38:39]
	v_mov_b64_e32 v[8:9], v[40:41]
	v_mov_b64_e32 v[10:11], v[42:43]
	v_mov_b64_e32 v[12:13], v[44:45]
	v_mov_b64_e32 v[14:15], v[46:47]
	s_bitcmp1_b32 s96, 7
	s_cbranch_scc0 .Lstg_m1_pre
	s_waitcnt vmcnt(0)
	s_barrier

; #define LAS __attribute__((address_space(3)))
; __device__ __forceinline__ float fast_exp2(float x) { return __builtin_amdgcn_exp2f(x); }
;     ...
;         if (!first) { const float f = fast_exp2(-dl); l *= f;
;             if (hi == 0) wsf[r32] = f;
;             asm volatile("s_waitcnt lgkmcnt(0)" ::: "memory");
; #pragma unroll
;             for (int g = 0; g < 4; ++g) { const f32x4 a = *(const LAS f32x4*)(wsf + 8 * g + 4 * hi);
; #pragma unroll
;                 for (int db = 0; db < DH / 32; ++db) { o[db][4 * g + 0] *= a[0]; o[db][4 * g + 1] *= a[1]; o[db][4 * g + 2] *= a[2]; o[db][4 * g + 3] *= a[3]; } }
; __device__ __forceinline__ void moba_unit(const MobaArgs& A, int b, int h, int qb, LAS unsigned char* lds, int wave, bool tables) {
;     ...
;         if (j + 1 < NP) { const int j1 = j + 1; const int kt1 = (j1 < 2) ? q0 + 128 * j1 : 256 * (qb - 1 - ((j1 - 2) >> 1)) + 128 * ((j1 - 2) & 1);
;             LAS unsigned char* sl = lds + L_BUF + (j1 & 1) * 32768;
;             stage_tile<64>(sl, Kh + (size_t)kt1 * 512, Vh + (size_t)kt1 * 512, 512, 512, wid, lane);
;             stage_tile<64>(sl + 16384, Kh + (size_t)(kt1 + 64) * 512, Vh + (size_t)(kt1 + 64) * 512, 512, 512, wid, lane); }
;         const bool own = j < 2; const int blk = own ? qb : qb - 1 - ((j - 2) >> 1); const int kt0 = own ? q0 + 128 * j : 256 * blk + 128 * ((j - 2) & 1);
;         const bool sel = own || ((selmask >> blk) & 1u);
;         const bool skip = (own ? (kt0 > qmin + 31) : !__any(sel)) || A.abl == 5;
.Lstg_m1_skip:
	s_bitcmp1_b32 s96, 7
	s_cbranch_scc0 .Lstg_m1_s_a
	s_waitcnt vmcnt(0)
	s_barrier
	s_branch .Lstg_m1_s_done
.Lstg_m1_s_a:
	s_barrier
	s_add_i32 s6, s84, 3
	s_cmp_ge_u32 s6, s95
	s_cbranch_scc1 .Lstg_m1_s_done
	s_cmp_eq_u32 s84, -2
	s_mov_b32 s6, s86
	s_cbranch_scc1 .Lstg_m1_s_k
	s_add_i32 s6, s84, 1
	s_not_b32 s6, s6
	s_lshr_b32 s6, s6, 1
	s_add_i32 s6, s81, s6
	s_add_i32 s7, s97, 0xffffff80
	s_lshl_b32 s6, s6, 8
	s_and_b32 s7, s7, 0x80
	s_or_b32 s6, s6, s7
.Lstg_m1_s_k:
	s_add_i32 s7, s87, 0x8000
	s_and_b32 s8, s7, 0x8000
	s_ashr_i32 s7, s6, 31
	s_lshl_b64 s[6:7], s[6:7], 10
	s_add_i32 s8, s82, s8
	v_lshl_add_u64 v[214:215], v[136:137], 0, s[6:7]
	s_mov_b32 m0, s8
	s_nop 0
	global_load_lds_dwordx4 v[214:215], off
	s_add_i32 m0, s8, 0x2000
	v_lshl_add_u64 v[214:215], v[138:139], 0, s[6:7]
	s_add_u32 s6, s6, 0x10000
	s_addc_u32 s7, s7, 0
	global_load_lds_dwordx4 v[214:215], off
	v_lshl_add_u64 v[214:215], v[136:137], 0, s[6:7]
	s_add_i32 m0, s8, 0x4000
	s_nop 0
	global_load_lds_dwordx4 v[214:215], off
	v_lshl_add_u64 v[214:215], v[138:139], 0, s[6:7]
	s_add_i32 m0, s8, 0x6000
	s_nop 0
	global_load_lds_dwordx4 v[214:215], off
.Lstg_m1_s_done:
	s_branch .LBB0_647
.LBB0_644:
	s_or_b64 exec, exec, s[6:7]
	v_mul_f32_e32 v162, v162, v141
	s_waitcnt lgkmcnt(0)
	v_add_u32_e32 v141, s3, v132
	ds_read_b128 v[142:145], v141
	ds_read_b128 v[146:149], v141 offset:32
	ds_read_b128 v[150:153], v141 offset:64
	ds_read_b128 v[168:171], v141 offset:96
	s_waitcnt lgkmcnt(0)
	v_pk_mul_f32 v[18:19], v[18:19], v[144:145]
	v_pk_mul_f32 v[20:21], v[20:21], v[146:147]
	v_pk_mul_f32 v[24:25], v[24:25], v[150:151]
	v_pk_mul_f32 v[28:29], v[28:29], v[168:169]
	v_pk_mul_f32 v[30:31], v[30:31], v[170:171]
	v_pk_mul_f32 v[26:27], v[26:27], v[152:153]
	v_pk_mul_f32 v[22:23], v[22:23], v[148:149]
	v_pk_mul_f32 v[16:17], v[16:17], v[142:143]
	v_pk_mul_f32 v[12:13], v[12:13], v[168:169]
	v_pk_mul_f32 v[8:9], v[8:9], v[150:151]
	v_pk_mul_f32 v[4:5], v[4:5], v[146:147]
	v_pk_mul_f32 v[14:15], v[14:15], v[170:171]
	v_pk_mul_f32 v[10:11], v[10:11], v[152:153]
	v_pk_mul_f32 v[6:7], v[6:7], v[148:149]
	v_pk_mul_f32 v[2:3], v[2:3], v[144:145]
	v_pk_mul_f32 v[0:1], v[0:1], v[142:143]

; __device__ __forceinline__ float fast_exp2(float x) { return __builtin_amdgcn_exp2f(x); }
; __device__ __forceinline__ void softmax_pv2(f32x16& a0, f32x16& a1, f32x16& b0, f32x16& b1, f32x16 (&o)[2], float& mref, float& l, f32x16& cn, bool first, LAS float* wsf, ...
;     ...
;     float s0 = 0.f, s1 = 0.f, s2 = 0.f, s3 = 0.f;
; #pragma unroll
;     for (int r = 0; r < 16; ++r) { a0[r] = fast_exp2(a0[r]); a1[r] = fast_exp2(a1[r]); b0[r] = fast_exp2(b0[r]); b1[r] = fast_exp2(b1[r]); s0 += a0[r]; s1 += a1[r]; s2 += b0[r]; s3 += b1[r]; }
.LBB0_646:
	v_exp_f32_e32 v141, v80
	v_exp_f32_e32 v143, v64
	v_exp_f32_e32 v142, v96
	v_exp_f32_e32 v140, v48
	v_exp_f32_e32 v81, v81
	v_exp_f32_e32 v65, v65
	v_exp_f32_e32 v64, v97
	v_exp_f32_e32 v80, v49
	v_exp_f32_e32 v97, v82
	v_exp_f32_e32 v145, v66
	v_exp_f32_e32 v144, v98
	v_exp_f32_e32 v96, v50
	v_exp_f32_e32 v83, v83
	v_exp_f32_e32 v67, v67
	v_exp_f32_e32 v66, v99
	v_exp_f32_e32 v82, v51
	v_exp_f32_e32 v99, v84
	v_exp_f32_e32 v147, v68
	v_exp_f32_e32 v146, v100
	v_exp_f32_e32 v98, v52
	s_bitcmp1_b32 s96, 7
	s_cbranch_scc0 .Lstg_m1_x_a
	s_waitcnt vmcnt(0)
	s_barrier
	s_branch .Lstg_m1_x_done

; #define LAS __attribute__((address_space(3)))
; __device__ __forceinline__ float fast_exp2(float x) { return __builtin_amdgcn_exp2f(x); }
; __device__ __forceinline__ s16x4 vtr(const LAS unsigned char* p) { return __builtin_bit_cast(s16x4, __builtin_amdgcn_ds_read_tr16_b64_v4i16((LAS v4i16_t*)p)); }
; #define PK8(P, B) __builtin_bit_cast(bf16x8, (u32x4){pk_bf16(P[B], P[B + 1]), pk_bf16(P[B + 2], P[B + 3]), pk_bf16(P[B + 4], P[B + 5]), pk_bf16(P[B + 6], P[B + 7])})
; __device__ __forceinline__ void softmax_pv2(f32x16& a0, f32x16& a1, f32x16& b0, f32x16& b1, f32x16 (&o)[2], float& mref, float& l, f32x16& cn, bool first, LAS float* wsf, ...
;     ...
;     float s0 = 0.f, s1 = 0.f, s2 = 0.f, s3 = 0.f;
; #pragma unroll
;     for (int r = 0; r < 16; ++r) { a0[r] = fast_exp2(a0[r]); a1[r] = fast_exp2(a1[r]); b0[r] = fast_exp2(b0[r]); b1[r] = fast_exp2(b1[r]); s0 += a0[r]; s1 += a1[r]; s2 += b0[r]; s3 += b1[r]; }
;     l += (s0 + s1) + (s2 + s3);
;     bf16x8 pa[8];
;     ...
;     pa[0] = PK8(a0, 0); pa[1] = PK8(a0, 8); pa[2] = PK8(a1, 0); pa[3] = PK8(a1, 8); pa[4] = PK8(b0, 0); pa[5] = PK8(b0, 8); pa[6] = PK8(b1, 0); pa[7] = PK8(b1, 8);
;     ...
;     const int voff = (4 * hi + ((lane & 15) >> 2)) * 64 + ((lane >> 4) & 1) * 32 + (lane & 3) * 8;
; #pragma unroll
;     for (int t = 0; t < 2; ++t) { const LAS unsigned char* vb = (t == 0 ? VsA : VsB) + voff;
;         s16x4 lo[8], hh[8];
; #pragma unroll
;         for (int db = 0; db < 2; ++db)
; #pragma unroll
;             for (int ks = 0; ks < 4; ++ks) { lo[db * 4 + ks] = vtr(vb + db * 4096 + ks * 1024); hh[db * 4 + ks] = vtr(vb + db * 4096 + ks * 1024 + 512); }
;         __builtin_amdgcn_sched_barrier(0);
;     #pragma unroll
;         for (int ks = 0; ks < 4; ++ks)
; #pragma unroll
;             for (int db = 0; db < 2; ++db) { const int i = db * 4 + ks;
;                 const bf16x8 vf = (bf16x8){lo[i][0], lo[i][1], lo[i][2], lo[i][3], hh[i][0], hh[i][1], hh[i][2], hh[i][3]};
;                 o[db] = __builtin_amdgcn_mfma_f32_32x32x16_bf16(pa[4 * t + ks], vf, o[db], 0, 0, 0); }
;         }
.Lstg_m1_x_done:
	v_pk_add_f32 v[48:49], v[142:143], 0 op_sel_hi:[1,0]
	v_pk_add_f32 v[50:51], v[140:141], 0 op_sel_hi:[1,0]
	v_pk_add_f32 v[48:49], v[64:65], v[48:49]
	v_pk_add_f32 v[50:51], v[80:81], v[50:51]
	v_exp_f32_e32 v85, v85
	v_exp_f32_e32 v69, v69
	v_exp_f32_e32 v68, v101
	v_exp_f32_e32 v84, v53
	v_pk_add_f32 v[48:49], v[144:145], v[48:49]
	v_pk_add_f32 v[50:51], v[96:97], v[50:51]
	v_exp_f32_e32 v101, v86
	v_exp_f32_e32 v149, v70
	v_exp_f32_e32 v148, v102
	v_exp_f32_e32 v100, v54
	v_pk_add_f32 v[48:49], v[66:67], v[48:49]
	v_pk_add_f32 v[50:51], v[82:83], v[50:51]
	v_exp_f32_e32 v87, v87
	v_exp_f32_e32 v71, v71
	v_exp_f32_e32 v70, v103
	v_exp_f32_e32 v86, v55
	v_pk_add_f32 v[48:49], v[146:147], v[48:49]
	v_pk_add_f32 v[50:51], v[98:99], v[50:51]
	v_exp_f32_e32 v151, v88
	v_exp_f32_e32 v103, v72
	v_exp_f32_e32 v102, v104
	v_exp_f32_e32 v150, v56
	v_exp_f32_e32 v153, v89
	v_exp_f32_e32 v73, v73
	v_exp_f32_e32 v72, v105
	v_exp_f32_e32 v152, v57
	v_pk_add_f32 v[48:49], v[68:69], v[48:49]
	v_pk_add_f32 v[50:51], v[84:85], v[50:51]
	v_exp_f32_e32 v169, v90
	v_exp_f32_e32 v89, v74
	v_exp_f32_e32 v88, v106
	v_exp_f32_e32 v168, v58
	v_pk_add_f32 v[48:49], v[148:149], v[48:49]
	v_pk_add_f32 v[50:51], v[100:101], v[50:51]
	v_exp_f32_e32 v171, v91
	v_exp_f32_e32 v75, v75
	v_exp_f32_e32 v74, v107
	v_exp_f32_e32 v170, v59
	v_pk_add_f32 v[48:49], v[70:71], v[48:49]
	v_pk_add_f32 v[50:51], v[86:87], v[50:51]
	v_exp_f32_e32 v173, v92
	v_exp_f32_e32 v91, v76
	v_exp_f32_e32 v90, v108
	v_exp_f32_e32 v172, v60
	v_pk_add_f32 v[48:49], v[102:103], v[48:49]
	v_pk_add_f32 v[50:51], v[150:151], v[50:51]
	v_exp_f32_e32 v175, v93
	v_exp_f32_e32 v77, v77
	v_exp_f32_e32 v76, v109
	v_exp_f32_e32 v174, v61
	v_pk_add_f32 v[48:49], v[72:73], v[48:49]
	v_pk_add_f32 v[50:51], v[152:153], v[50:51]
	v_exp_f32_e32 v177, v94
	v_exp_f32_e32 v93, v78
	v_exp_f32_e32 v92, v110
	v_exp_f32_e32 v176, v62
	v_pk_add_f32 v[48:49], v[88:89], v[48:49]
	v_pk_add_f32 v[50:51], v[168:169], v[50:51]
	v_exp_f32_e32 v179, v95
	v_exp_f32_e32 v79, v79
	v_exp_f32_e32 v78, v111
	v_exp_f32_e32 v178, v63
	v_pk_add_f32 v[48:49], v[74:75], v[48:49]
	v_pk_add_f32 v[50:51], v[170:171], v[50:51]
	v_pk_add_f32 v[48:49], v[90:91], v[48:49]
	v_pk_add_f32 v[50:51], v[172:173], v[50:51]
	v_pk_add_f32 v[48:49], v[76:77], v[48:49]
	v_pk_add_f32 v[50:51], v[174:175], v[50:51]
	v_pk_add_f32 v[48:49], v[92:93], v[48:49]
	v_pk_add_f32 v[50:51], v[176:177], v[50:51]
	v_pk_add_f32 v[48:49], v[78:79], v[48:49]
	v_pk_add_f32 v[50:51], v[178:179], v[50:51]
	v_cvt_pk_bf16_f32 v57, v145, v67
	v_pk_add_f32 v[48:49], v[50:51], v[48:49]
	v_cvt_pk_bf16_f32 v67, v148, v70
	v_cvt_pk_bf16_f32 v70, v90, v76
	v_add3_u32 v76, s94, v161, v163
	v_add_f32_e32 v48, v48, v49
	v_cvt_pk_bf16_f32 v56, v143, v65
	v_cvt_pk_bf16_f32 v65, v144, v66
	v_cvt_pk_bf16_f32 v66, v146, v68
	v_cvt_pk_bf16_f32 v68, v102, v72
	v_cvt_pk_bf16_f32 v72, v140, v80
	v_add3_u32 v140, v76, v165, v157
	v_add_f32_e32 v162, v162, v48
	v_cvt_pk_bf16_f32 v48, v141, v81
	v_cvt_pk_bf16_f32 v49, v97, v83
	v_cvt_pk_bf16_f32 v50, v99, v85
	v_cvt_pk_bf16_f32 v51, v101, v87
	v_cvt_pk_bf16_f32 v58, v147, v69
	v_cvt_pk_bf16_f32 v59, v149, v71
	v_cvt_pk_bf16_f32 v60, v103, v73
	v_cvt_pk_bf16_f32 v61, v89, v75
	v_cvt_pk_bf16_f32 v62, v91, v77
	v_cvt_pk_bf16_f32 v63, v93, v79
	v_cvt_pk_bf16_f32 v69, v88, v74
	v_cvt_pk_bf16_f32 v71, v92, v78
	v_cvt_pk_bf16_f32 v73, v96, v82
	v_cvt_pk_bf16_f32 v74, v98, v84
	v_cvt_pk_bf16_f32 v75, v100, v86
	ds_read_b64_tr_b16 v[76:77], v140 offset:8192
	ds_read_b64_tr_b16 v[78:79], v140 offset:8704
	ds_read_b64_tr_b16 v[80:81], v140 offset:9216
	ds_read_b64_tr_b16 v[82:83], v140 offset:9728
	ds_read_b64_tr_b16 v[84:85], v140 offset:10240
	ds_read_b64_tr_b16 v[86:87], v140 offset:10752
	ds_read_b64_tr_b16 v[88:89], v140 offset:11264
	ds_read_b64_tr_b16 v[90:91], v140 offset:11776
	ds_read_b64_tr_b16 v[92:93], v140 offset:12288
	ds_read_b64_tr_b16 v[94:95], v140 offset:12800
	ds_read_b64_tr_b16 v[96:97], v140 offset:13312
	ds_read_b64_tr_b16 v[98:99], v140 offset:13824
	ds_read_b64_tr_b16 v[100:101], v140 offset:14336
	ds_read_b64_tr_b16 v[102:103], v140 offset:14848
	ds_read_b64_tr_b16 v[104:105], v140 offset:15360
	ds_read_b64_tr_b16 v[106:107], v140 offset:15872
	v_cvt_pk_bf16_f32 v52, v151, v153
	v_cvt_pk_bf16_f32 v53, v169, v171
	v_cvt_pk_bf16_f32 v54, v173, v175
	v_cvt_pk_bf16_f32 v55, v177, v179
	v_cvt_pk_bf16_f32 v64, v142, v64
	v_cvt_pk_bf16_f32 v108, v150, v152
	v_cvt_pk_bf16_f32 v109, v168, v170
	v_cvt_pk_bf16_f32 v110, v172, v174
	v_cvt_pk_bf16_f32 v111, v176, v178
	s_waitcnt lgkmcnt(14)
	v_mfma_f32_32x32x16_bf16 v[16:31], v[48:51], v[76:79], v[16:31]
	s_waitcnt lgkmcnt(6)
	v_mfma_f32_32x32x16_bf16 v[0:15], v[48:51], v[92:95], v[0:15]
	v_mfma_f32_32x32x16_bf16 v[16:31], v[52:55], v[80:83], v[16:31]
	s_waitcnt lgkmcnt(4)
	v_mfma_f32_32x32x16_bf16 v[0:15], v[52:55], v[96:99], v[0:15]
	v_mfma_f32_32x32x16_bf16 v[16:31], v[56:59], v[84:87], v[16:31]
	s_waitcnt lgkmcnt(2)
	v_mfma_f32_32x32x16_bf16 v[0:15], v[56:59], v[100:103], v[0:15]
	ds_read_b64_tr_b16 v[48:49], v140 offset:24576
	ds_read_b64_tr_b16 v[50:51], v140 offset:25088
	ds_read_b64_tr_b16 v[52:53], v140 offset:25600
	ds_read_b64_tr_b16 v[54:55], v140 offset:26112
	ds_read_b64_tr_b16 v[56:57], v140 offset:26624
	ds_read_b64_tr_b16 v[58:59], v140 offset:27136
	ds_read_b64_tr_b16 v[76:77], v140 offset:27648
	ds_read_b64_tr_b16 v[78:79], v140 offset:28160
	v_mfma_f32_32x32x16_bf16 v[16:31], v[60:63], v[88:91], v[16:31]
	ds_read_b64_tr_b16 v[80:81], v140 offset:28672
	ds_read_b64_tr_b16 v[82:83], v140 offset:29184
	ds_read_b64_tr_b16 v[84:85], v140 offset:29696
	ds_read_b64_tr_b16 v[86:87], v140 offset:30208
	ds_read_b64_tr_b16 v[88:89], v140 offset:30720
	ds_read_b64_tr_b16 v[90:91], v140 offset:31232
	ds_read_b64_tr_b16 v[92:93], v140 offset:31744
	ds_read_b64_tr_b16 v[94:95], v140 offset:32256
	s_waitcnt lgkmcnt(14)
	v_mfma_f32_32x32x16_bf16 v[0:15], v[60:63], v[104:107], v[0:15]
	v_mfma_f32_32x32x16_bf16 v[16:31], v[64:67], v[48:51], v[16:31]
	s_waitcnt lgkmcnt(6)
	v_mfma_f32_32x32x16_bf16 v[0:15], v[64:67], v[80:83], v[0:15]
	v_mfma_f32_32x32x16_bf16 v[16:31], v[68:71], v[52:55], v[16:31]
	s_waitcnt lgkmcnt(4)
	v_mfma_f32_32x32x16_bf16 v[0:15], v[68:71], v[84:87], v[0:15]
	v_mfma_f32_32x32x16_bf16 v[16:31], v[72:75], v[56:59], v[16:31]
	s_waitcnt lgkmcnt(2)
	v_mfma_f32_32x32x16_bf16 v[0:15], v[72:75], v[88:91], v[0:15]
	v_mfma_f32_32x32x16_bf16 v[16:31], v[108:111], v[76:79], v[16:31]
	s_waitcnt lgkmcnt(0)
	v_mfma_f32_32x32x16_bf16 v[0:15], v[108:111], v[92:95], v[0:15]

; #define LAS __attribute__((address_space(3)))
; __device__ __forceinline__ void moba_unit(const MobaArgs& A, int b, int h, int qb, LAS unsigned char* lds, int wave, bool tables) {
;     ...
;         asm volatile("s_waitcnt vmcnt(0)" ::: "memory");
;         __syncthreads();
;         if (j + 1 < NP) { const int j1 = j + 1; const int kt1 = (j1 < 2) ? q0 + 128 * j1 : 256 * (qb - 1 - ((j1 - 2) >> 1)) + 128 * ((j1 - 2) & 1);
;             LAS unsigned char* sl = lds + L_BUF + (j1 & 1) * 32768;
;             stage_tile<64>(sl, Kh + (size_t)kt1 * 512, Vh + (size_t)kt1 * 512, 512, 512, wid, lane);
;             stage_tile<64>(sl + 16384, Kh + (size_t)(kt1 + 64) * 512, Vh + (size_t)(kt1 + 64) * 512, 512, 512, wid, lane); }
.LBB0_648:
	s_waitcnt vmcnt(0)
	s_add_i32 s6, s84, 3
	s_cmp_ge_u32 s6, s95
	s_waitcnt vmcnt(0) lgkmcnt(0)
	s_barrier
	s_cbranch_scc1 .LBB0_652
	s_bitcmp1_b32 s96, 7
	s_cbranch_scc0 .LBB0_652
	s_cmp_eq_u32 s84, -2
	s_mov_b32 s6, s86
	s_cbranch_scc1 .LBB0_651
	s_add_i32 s6, s84, 1
	s_not_b32 s6, s6
	s_lshr_b32 s6, s6, 1
	s_add_i32 s6, s81, s6
	s_add_i32 s7, s97, 0xffffff80
	s_lshl_b32 s6, s6, 8
	s_and_b32 s7, s7, 0x80
	s_or_b32 s6, s6, s7

; __device__ __forceinline__ float fast_rcp(float x) { return __builtin_amdgcn_rcpf(x); }
; __device__ __forceinline__ void moba_unit(const MobaArgs& A, int b, int h, int qb, LAS unsigned char* lds, int wave, bool tables) {
;     ...
;     }
;     ...
;     if (A.stamp != nullptr && tid == 0) { const unsigned long long tot = __builtin_readcyclecounter() - tu0_; *A.stamp = __float_as_uint(20.0f + ((float)tot - 150000.0f) * (1.0f / 500.0f)); }
;     ...
;     const float lt = l + __shfl_xor(l, 32);
;     if (!A.dry) store_o<64>(o, fast_rcp(lt), wsf, ost, A.O + (rowb + q0 + 32 * wid) * 512 + h * HD, 512, lane, r32, hi);
.LBB0_678:
	s_bitcmp1_b32 s96, 7
	s_cbranch_scc1 .Lstg_m1_ex
	s_barrier

; __device__ __forceinline__ void moba_unit(const MobaArgs& A, int b, int h, int qb, LAS unsigned char* lds, int wave, bool tables) {
;     ...
;     float mref = 0.f, l = 0.f; f32x16 o[2], cn;
;     float zf = 0.f; asm volatile("" : "+v"(zf));
; #pragma unroll
;     for (int r = 0; r < 16; ++r) { o[0][r] = zf; o[1][r] = zf; cn[r] = zf; }
;     const int NP = 2 * (qb + 1); const int qmin = q0 + 32 * wid;
;     const float bfar = lut[LUTA_TOP - 1000];
;     stage_tile<64>(lds + L_BUF + 16384, Kh + (size_t)(q0 + 64) * 512, Vh + (size_t)(q0 + 64) * 512, 512, 512, wid, lane);
.LBB0_721:
	s_and_b32 s3, s3, 0x3fffffc0
	s_lshl_b32 s3, s3, 2
	s_add_i32 s3, s3, 0
	s_add_i32 s3, s3, 0x13000
	s_add_i32 s76, s71, 2
	s_bitset1_b32 s22, 16
	s_add_u32 s4, s72, s22
	v_lshlrev_b32_e32 v1, 9, v152
	s_addc_u32 s5, s73, 0
	s_add_u32 s6, s74, s22
	v_lshlrev_b32_e32 v2, 1, v1
	v_mov_b32_e32 v3, v113
	v_lshlrev_b32_e32 v0, 9, v32
	s_addc_u32 s7, s75, 0
	v_lshl_add_u64 v[4:5], s[4:5], 0, v[2:3]
	s_lshl_b64 s[4:5], s[10:11], 1
	v_mov_b32_e32 v32, v113
	v_lshl_add_u64 v[4:5], v[4:5], 0, s[4:5]
	s_add_i32 m0, s81, 0x4000
	v_lshlrev_b32_e32 v0, 1, v0
	v_mov_b32_e32 v1, v113
	global_load_lds_dwordx4 v[4:5], off
	v_lshl_add_u64 v[4:5], s[6:7], 0, v[0:1]
	s_lshl_b64 s[6:7], s[12:13], 1
	v_lshl_add_u64 v[4:5], v[4:5], 0, s[6:7]
	v_lshl_add_u64 v[4:5], v[4:5], 0, v[112:113]
	s_add_i32 m0, s81, 0x6000
	v_readlane_b32 s8, v254, 12
	global_load_lds_dwordx4 v[4:5], off
	s_nop 0
	v_mov_b32_e32 v4, s8
	v_lshl_add_u64 v[0:1], s[74:75], 0, v[0:1]
	ds_read_b32 v133, v4
	v_lshl_add_u64 v[0:1], v[0:1], 0, s[6:7]
	v_lshl_add_u64 v[136:137], v[0:1], 0, v[112:113]
	v_lshlrev_b32_e32 v0, 4, v152
	v_mov_b32_e32 v33, v32
	v_lshl_add_u64 v[2:3], s[72:73], 0, v[2:3]
	v_and_b32_e32 v163, 0xc0, v0
	v_lshlrev_b32_e32 v0, 1, v152
	v_mov_b32_e32 v34, v32
	v_mov_b32_e32 v35, v32
	v_mov_b32_e32 v36, v32
	v_mov_b32_e32 v37, v32
	v_mov_b32_e32 v38, v32
	v_mov_b32_e32 v39, v32
	v_mov_b32_e32 v40, v32
	v_mov_b32_e32 v41, v32
	v_mov_b32_e32 v42, v32
	v_mov_b32_e32 v43, v32
	v_mov_b32_e32 v44, v32
	v_mov_b32_e32 v45, v32
	v_mov_b32_e32 v46, v32
	v_mov_b32_e32 v47, v32
	v_lshl_add_u64 v[134:135], v[2:3], 0, s[4:5]
	v_and_b32_e32 v165, 32, v0
	v_readlane_b32 s6, v254, 13
	v_mov_b64_e32 v[16:17], v[32:33]
	v_mov_b64_e32 v[0:1], v[32:33]
	s_mov_b32 s77, 0
	s_or_b32 s62, s79, 0x80
	s_or_b32 s63, s92, 31
	v_lshlrev_b32_e32 v158, 10, v156
	v_lshlrev_b32_e32 v159, 4, v155
	v_lshlrev_b32_e32 v160, 2, v156
	v_cmp_gt_u32_e64 s[4:5], 32, v152
	v_lshl_add_u32 v112, v155, 2, s3
	v_lshlrev_b32_e32 v162, 8, v156
	v_add_u32_e32 v166, s6, v130
	v_mov_b32_e32 v161, 0
	s_mov_b32 s72, -2
	s_mov_b32 s73, 0
	v_mov_b64_e32 v[18:19], v[34:35]
	v_mov_b64_e32 v[20:21], v[36:37]
	v_mov_b64_e32 v[22:23], v[38:39]
	v_mov_b64_e32 v[24:25], v[40:41]
	v_mov_b64_e32 v[26:27], v[42:43]
	v_mov_b64_e32 v[28:29], v[44:45]
	v_mov_b64_e32 v[30:31], v[46:47]
	v_mov_b64_e32 v[2:3], v[34:35]
	v_mov_b64_e32 v[4:5], v[36:37]
	v_mov_b64_e32 v[6:7], v[38:39]
	v_mov_b64_e32 v[8:9], v[40:41]
	v_mov_b64_e32 v[10:11], v[42:43]
	v_mov_b64_e32 v[12:13], v[44:45]
	v_mov_b64_e32 v[14:15], v[46:47]
	v_readlane_b32 s75, v255, 13
	s_bitcmp1_b32 s92, 7
	s_cbranch_scc0 .Lstg_m2_pre
	s_waitcnt vmcnt(0)
	s_barrier

; #define LAS __attribute__((address_space(3)))
; __device__ __forceinline__ float fast_exp2(float x) { return __builtin_amdgcn_exp2f(x); }
;     ...
;         if (!first) { const float f = fast_exp2(-dl); l *= f;
;             if (hi == 0) wsf[r32] = f;
;             asm volatile("s_waitcnt lgkmcnt(0)" ::: "memory");
; #pragma unroll
;             for (int g = 0; g < 4; ++g) { const f32x4 a = *(const LAS f32x4*)(wsf + 8 * g + 4 * hi);
; #pragma unroll
;                 for (int db = 0; db < DH / 32; ++db) { o[db][4 * g + 0] *= a[0]; o[db][4 * g + 1] *= a[1]; o[db][4 * g + 2] *= a[2]; o[db][4 * g + 3] *= a[3]; } }
; __device__ __forceinline__ void moba_unit(const MobaArgs& A, int b, int h, int qb, LAS unsigned char* lds, int wave, bool tables) {
;     ...
;         if (j + 1 < NP) { const int j1 = j + 1; const int kt1 = (j1 < 2) ? q0 + 128 * j1 : 256 * (qb - 1 - ((j1 - 2) >> 1)) + 128 * ((j1 - 2) & 1);
;             LAS unsigned char* sl = lds + L_BUF + (j1 & 1) * 32768;
;             stage_tile<64>(sl, Kh + (size_t)kt1 * 512, Vh + (size_t)kt1 * 512, 512, 512, wid, lane);
;             stage_tile<64>(sl + 16384, Kh + (size_t)(kt1 + 64) * 512, Vh + (size_t)(kt1 + 64) * 512, 512, 512, wid, lane); }
;         const bool own = j < 2; const int blk = own ? qb : qb - 1 - ((j - 2) >> 1); const int kt0 = own ? q0 + 128 * j : 256 * blk + 128 * ((j - 2) & 1);
;         const bool sel = own || ((selmask >> blk) & 1u);
;         const bool skip = (own ? (kt0 > qmin + 31) : !__any(sel)) || A.abl == 5;
.Lstg_m2_skip:
	s_bitcmp1_b32 s92, 7
	s_cbranch_scc0 .Lstg_m2_s_a
	s_waitcnt vmcnt(0)
	s_barrier
	s_branch .Lstg_m2_s_done
.Lstg_m2_s_a:
	s_barrier
	s_add_i32 s6, s72, 3
	s_cmp_ge_u32 s6, s76
	s_cbranch_scc1 .Lstg_m2_s_done
	s_cmp_eq_u32 s72, -2
	s_mov_b32 s6, s62
	s_cbranch_scc1 .Lstg_m2_s_k
	s_add_i32 s6, s72, 1
	s_not_b32 s6, s6
	s_lshr_b32 s6, s6, 1
	s_add_i32 s6, s89, s6
	s_add_i32 s7, s73, 0xffffff80
	s_lshl_b32 s6, s6, 8
	s_and_b32 s7, s7, 0x80
	s_or_b32 s6, s6, s7
.Lstg_m2_s_k:
	s_add_i32 s7, s77, 0x8000
	s_and_b32 s8, s7, 0x8000
	s_ashr_i32 s7, s6, 31
	s_lshl_b64 s[6:7], s[6:7], 10
	s_add_i32 s8, s81, s8
	v_lshl_add_u64 v[214:215], v[134:135], 0, s[6:7]
	s_mov_b32 m0, s8
	s_nop 0
	global_load_lds_dwordx4 v[214:215], off
	s_add_i32 m0, s8, 0x2000
	v_lshl_add_u64 v[214:215], v[136:137], 0, s[6:7]
	s_add_u32 s6, s6, 0x10000
	s_addc_u32 s7, s7, 0
	global_load_lds_dwordx4 v[214:215], off
	v_lshl_add_u64 v[214:215], v[134:135], 0, s[6:7]
	s_add_i32 m0, s8, 0x4000
	s_nop 0
	global_load_lds_dwordx4 v[214:215], off
	v_lshl_add_u64 v[214:215], v[136:137], 0, s[6:7]
	s_add_i32 m0, s8, 0x6000
	s_nop 0
	global_load_lds_dwordx4 v[214:215], off
.Lstg_m2_s_done:
	s_branch .LBB0_725
.LBB0_722:
	s_or_b64 exec, exec, s[6:7]
	v_mul_f32_e32 v161, v161, v139
	s_waitcnt lgkmcnt(0)
	v_add_u32_e32 v139, s3, v130
	ds_read_b128 v[140:143], v139
	ds_read_b128 v[144:147], v139 offset:32
	ds_read_b128 v[148:151], v139 offset:64
	ds_read_b128 v[168:171], v139 offset:96
	s_waitcnt lgkmcnt(0)
	v_pk_mul_f32 v[18:19], v[18:19], v[142:143]
	v_pk_mul_f32 v[20:21], v[20:21], v[144:145]
	v_pk_mul_f32 v[24:25], v[24:25], v[148:149]
	v_pk_mul_f32 v[28:29], v[28:29], v[168:169]
	v_pk_mul_f32 v[30:31], v[30:31], v[170:171]
	v_pk_mul_f32 v[26:27], v[26:27], v[150:151]
	v_pk_mul_f32 v[22:23], v[22:23], v[146:147]
	v_pk_mul_f32 v[16:17], v[16:17], v[140:141]
	v_pk_mul_f32 v[12:13], v[12:13], v[168:169]
	v_pk_mul_f32 v[8:9], v[8:9], v[148:149]
	v_pk_mul_f32 v[4:5], v[4:5], v[144:145]
	v_pk_mul_f32 v[14:15], v[14:15], v[170:171]
	v_pk_mul_f32 v[10:11], v[10:11], v[150:151]
	v_pk_mul_f32 v[6:7], v[6:7], v[146:147]
	v_pk_mul_f32 v[2:3], v[2:3], v[142:143]
	v_pk_mul_f32 v[0:1], v[0:1], v[140:141]

; __device__ __forceinline__ float fast_exp2(float x) { return __builtin_amdgcn_exp2f(x); }
; __device__ __forceinline__ void softmax_pv2(f32x16& a0, f32x16& a1, f32x16& b0, f32x16& b1, f32x16 (&o)[2], float& mref, float& l, f32x16& cn, bool first, LAS float* wsf, ...
;     ...
;     float s0 = 0.f, s1 = 0.f, s2 = 0.f, s3 = 0.f;
; #pragma unroll
;     for (int r = 0; r < 16; ++r) { a0[r] = fast_exp2(a0[r]); a1[r] = fast_exp2(a1[r]); b0[r] = fast_exp2(b0[r]); b1[r] = fast_exp2(b1[r]); s0 += a0[r]; s1 += a1[r]; s2 += b0[r]; s3 += b1[r]; }
.LBB0_724:
	v_exp_f32_e32 v139, v80
	v_exp_f32_e32 v141, v64
	v_exp_f32_e32 v140, v96
	v_exp_f32_e32 v138, v48
	v_exp_f32_e32 v81, v81
	v_exp_f32_e32 v65, v65
	v_exp_f32_e32 v64, v97
	v_exp_f32_e32 v80, v49
	v_exp_f32_e32 v97, v82
	v_exp_f32_e32 v143, v66
	v_exp_f32_e32 v142, v98
	v_exp_f32_e32 v96, v50
	v_exp_f32_e32 v83, v83
	v_exp_f32_e32 v67, v67
	v_exp_f32_e32 v66, v99
	v_exp_f32_e32 v82, v51
	v_exp_f32_e32 v99, v84
	v_exp_f32_e32 v145, v68
	v_exp_f32_e32 v144, v100
	v_exp_f32_e32 v98, v52
	s_bitcmp1_b32 s92, 7
	s_cbranch_scc0 .Lstg_m2_x_a
	s_waitcnt vmcnt(0)
	s_barrier
	s_branch .Lstg_m2_x_done

; #define LAS __attribute__((address_space(3)))
; __device__ __forceinline__ float fast_exp2(float x) { return __builtin_amdgcn_exp2f(x); }
; __device__ __forceinline__ s16x4 vtr(const LAS unsigned char* p) { return __builtin_bit_cast(s16x4, __builtin_amdgcn_ds_read_tr16_b64_v4i16((LAS v4i16_t*)p)); }
; #define PK8(P, B) __builtin_bit_cast(bf16x8, (u32x4){pk_bf16(P[B], P[B + 1]), pk_bf16(P[B + 2], P[B + 3]), pk_bf16(P[B + 4], P[B + 5]), pk_bf16(P[B + 6], P[B + 7])})
; __device__ __forceinline__ void softmax_pv2(f32x16& a0, f32x16& a1, f32x16& b0, f32x16& b1, f32x16 (&o)[2], float& mref, float& l, f32x16& cn, bool first, LAS float* wsf, ...
;     ...
;     float s0 = 0.f, s1 = 0.f, s2 = 0.f, s3 = 0.f;
; #pragma unroll
;     for (int r = 0; r < 16; ++r) { a0[r] = fast_exp2(a0[r]); a1[r] = fast_exp2(a1[r]); b0[r] = fast_exp2(b0[r]); b1[r] = fast_exp2(b1[r]); s0 += a0[r]; s1 += a1[r]; s2 += b0[r]; s3 += b1[r]; }
;     l += (s0 + s1) + (s2 + s3);
;     bf16x8 pa[8];
;     ...
;     pa[0] = PK8(a0, 0); pa[1] = PK8(a0, 8); pa[2] = PK8(a1, 0); pa[3] = PK8(a1, 8); pa[4] = PK8(b0, 0); pa[5] = PK8(b0, 8); pa[6] = PK8(b1, 0); pa[7] = PK8(b1, 8);
;     ...
;     const int voff = (4 * hi + ((lane & 15) >> 2)) * 64 + ((lane >> 4) & 1) * 32 + (lane & 3) * 8;
; #pragma unroll
;     for (int t = 0; t < 2; ++t) { const LAS unsigned char* vb = (t == 0 ? VsA : VsB) + voff;
;         s16x4 lo[8], hh[8];
; #pragma unroll
;         for (int db = 0; db < 2; ++db)
; #pragma unroll
;             for (int ks = 0; ks < 4; ++ks) { lo[db * 4 + ks] = vtr(vb + db * 4096 + ks * 1024); hh[db * 4 + ks] = vtr(vb + db * 4096 + ks * 1024 + 512); }
;         __builtin_amdgcn_sched_barrier(0);
;     #pragma unroll
;         for (int ks = 0; ks < 4; ++ks)
; #pragma unroll
;             for (int db = 0; db < 2; ++db) { const int i = db * 4 + ks;
;                 const bf16x8 vf = (bf16x8){lo[i][0], lo[i][1], lo[i][2], lo[i][3], hh[i][0], hh[i][1], hh[i][2], hh[i][3]};
;                 o[db] = __builtin_amdgcn_mfma_f32_32x32x16_bf16(pa[4 * t + ks], vf, o[db], 0, 0, 0); }
;         }
.Lstg_m2_x_done:
	v_pk_add_f32 v[48:49], v[140:141], 0 op_sel_hi:[1,0]
	v_pk_add_f32 v[50:51], v[138:139], 0 op_sel_hi:[1,0]
	v_pk_add_f32 v[48:49], v[64:65], v[48:49]
	v_pk_add_f32 v[50:51], v[80:81], v[50:51]
	v_exp_f32_e32 v85, v85
	v_exp_f32_e32 v69, v69
	v_exp_f32_e32 v68, v101
	v_exp_f32_e32 v84, v53
	v_pk_add_f32 v[48:49], v[142:143], v[48:49]
	v_pk_add_f32 v[50:51], v[96:97], v[50:51]
	v_exp_f32_e32 v101, v86
	v_exp_f32_e32 v147, v70
	v_exp_f32_e32 v146, v102
	v_exp_f32_e32 v100, v54
	v_pk_add_f32 v[48:49], v[66:67], v[48:49]
	v_pk_add_f32 v[50:51], v[82:83], v[50:51]
	v_exp_f32_e32 v87, v87
	v_exp_f32_e32 v71, v71
	v_exp_f32_e32 v70, v103
	v_exp_f32_e32 v86, v55
	v_pk_add_f32 v[48:49], v[144:145], v[48:49]
	v_pk_add_f32 v[50:51], v[98:99], v[50:51]
	v_exp_f32_e32 v149, v88
	v_exp_f32_e32 v103, v72
	v_exp_f32_e32 v102, v104
	v_exp_f32_e32 v148, v56
	v_exp_f32_e32 v151, v89
	v_exp_f32_e32 v73, v73
	v_exp_f32_e32 v72, v105
	v_exp_f32_e32 v150, v57
	v_pk_add_f32 v[48:49], v[68:69], v[48:49]
	v_pk_add_f32 v[50:51], v[84:85], v[50:51]
	v_exp_f32_e32 v169, v90
	v_exp_f32_e32 v89, v74
	v_exp_f32_e32 v88, v106
	v_exp_f32_e32 v168, v58
	v_pk_add_f32 v[48:49], v[146:147], v[48:49]
	v_pk_add_f32 v[50:51], v[100:101], v[50:51]
	v_exp_f32_e32 v171, v91
	v_exp_f32_e32 v75, v75
	v_exp_f32_e32 v74, v107
	v_exp_f32_e32 v170, v59
	v_pk_add_f32 v[48:49], v[70:71], v[48:49]
	v_pk_add_f32 v[50:51], v[86:87], v[50:51]
	v_exp_f32_e32 v173, v92
	v_exp_f32_e32 v91, v76
	v_exp_f32_e32 v90, v108
	v_exp_f32_e32 v172, v60
	v_pk_add_f32 v[48:49], v[102:103], v[48:49]
	v_pk_add_f32 v[50:51], v[148:149], v[50:51]
	v_exp_f32_e32 v175, v93
	v_exp_f32_e32 v77, v77
	v_exp_f32_e32 v76, v109
	v_exp_f32_e32 v174, v61
	v_pk_add_f32 v[48:49], v[72:73], v[48:49]
	v_pk_add_f32 v[50:51], v[150:151], v[50:51]
	v_exp_f32_e32 v177, v94
	v_exp_f32_e32 v93, v78
	v_exp_f32_e32 v92, v110
	v_exp_f32_e32 v176, v62
	v_pk_add_f32 v[48:49], v[88:89], v[48:49]
	v_pk_add_f32 v[50:51], v[168:169], v[50:51]
	v_exp_f32_e32 v179, v95
	v_exp_f32_e32 v79, v79
	v_exp_f32_e32 v78, v111
	v_exp_f32_e32 v178, v63
	v_pk_add_f32 v[48:49], v[74:75], v[48:49]
	v_pk_add_f32 v[50:51], v[170:171], v[50:51]
	v_pk_add_f32 v[48:49], v[90:91], v[48:49]
	v_pk_add_f32 v[50:51], v[172:173], v[50:51]
	v_pk_add_f32 v[48:49], v[76:77], v[48:49]
	v_pk_add_f32 v[50:51], v[174:175], v[50:51]
	v_pk_add_f32 v[48:49], v[92:93], v[48:49]
	v_pk_add_f32 v[50:51], v[176:177], v[50:51]
	v_pk_add_f32 v[48:49], v[78:79], v[48:49]
	v_pk_add_f32 v[50:51], v[178:179], v[50:51]
	v_cvt_pk_bf16_f32 v57, v143, v67
	v_pk_add_f32 v[48:49], v[50:51], v[48:49]
	v_cvt_pk_bf16_f32 v67, v146, v70
	v_cvt_pk_bf16_f32 v70, v90, v76
	v_add3_u32 v76, s74, v162, v163
	v_add_f32_e32 v48, v48, v49
	v_cvt_pk_bf16_f32 v56, v141, v65
	v_cvt_pk_bf16_f32 v65, v142, v66
	v_cvt_pk_bf16_f32 v66, v144, v68
	v_cvt_pk_bf16_f32 v68, v102, v72
	v_cvt_pk_bf16_f32 v72, v138, v80
	v_add3_u32 v138, v76, v165, v157
	v_add_f32_e32 v161, v161, v48
	v_cvt_pk_bf16_f32 v48, v139, v81
	v_cvt_pk_bf16_f32 v49, v97, v83
	v_cvt_pk_bf16_f32 v50, v99, v85
	v_cvt_pk_bf16_f32 v51, v101, v87
	v_cvt_pk_bf16_f32 v58, v145, v69
	v_cvt_pk_bf16_f32 v59, v147, v71
	v_cvt_pk_bf16_f32 v60, v103, v73
	v_cvt_pk_bf16_f32 v61, v89, v75
	v_cvt_pk_bf16_f32 v62, v91, v77
	v_cvt_pk_bf16_f32 v63, v93, v79
	v_cvt_pk_bf16_f32 v69, v88, v74
	v_cvt_pk_bf16_f32 v71, v92, v78
	v_cvt_pk_bf16_f32 v73, v96, v82
	v_cvt_pk_bf16_f32 v74, v98, v84
	v_cvt_pk_bf16_f32 v75, v100, v86
	ds_read_b64_tr_b16 v[76:77], v138 offset:8192
	ds_read_b64_tr_b16 v[78:79], v138 offset:8704
	ds_read_b64_tr_b16 v[80:81], v138 offset:9216
	ds_read_b64_tr_b16 v[82:83], v138 offset:9728
	ds_read_b64_tr_b16 v[84:85], v138 offset:10240
	ds_read_b64_tr_b16 v[86:87], v138 offset:10752
	ds_read_b64_tr_b16 v[88:89], v138 offset:11264
	ds_read_b64_tr_b16 v[90:91], v138 offset:11776
	ds_read_b64_tr_b16 v[92:93], v138 offset:12288
	ds_read_b64_tr_b16 v[94:95], v138 offset:12800
	ds_read_b64_tr_b16 v[96:97], v138 offset:13312
	ds_read_b64_tr_b16 v[98:99], v138 offset:13824
	ds_read_b64_tr_b16 v[100:101], v138 offset:14336
	ds_read_b64_tr_b16 v[102:103], v138 offset:14848
	ds_read_b64_tr_b16 v[104:105], v138 offset:15360
	ds_read_b64_tr_b16 v[106:107], v138 offset:15872
	v_cvt_pk_bf16_f32 v52, v149, v151
	v_cvt_pk_bf16_f32 v53, v169, v171
	v_cvt_pk_bf16_f32 v54, v173, v175
	v_cvt_pk_bf16_f32 v55, v177, v179
	v_cvt_pk_bf16_f32 v64, v140, v64
	v_cvt_pk_bf16_f32 v108, v148, v150
	v_cvt_pk_bf16_f32 v109, v168, v170
	v_cvt_pk_bf16_f32 v110, v172, v174
	v_cvt_pk_bf16_f32 v111, v176, v178
	s_waitcnt lgkmcnt(14)
	v_mfma_f32_32x32x16_bf16 v[16:31], v[48:51], v[76:79], v[16:31]
	s_waitcnt lgkmcnt(6)
	v_mfma_f32_32x32x16_bf16 v[0:15], v[48:51], v[92:95], v[0:15]
	v_mfma_f32_32x32x16_bf16 v[16:31], v[52:55], v[80:83], v[16:31]
	s_waitcnt lgkmcnt(4)
	v_mfma_f32_32x32x16_bf16 v[0:15], v[52:55], v[96:99], v[0:15]
	v_mfma_f32_32x32x16_bf16 v[16:31], v[56:59], v[84:87], v[16:31]
	s_waitcnt lgkmcnt(2)
	v_mfma_f32_32x32x16_bf16 v[0:15], v[56:59], v[100:103], v[0:15]
	ds_read_b64_tr_b16 v[48:49], v138 offset:24576
	ds_read_b64_tr_b16 v[50:51], v138 offset:25088
	ds_read_b64_tr_b16 v[52:53], v138 offset:25600
	ds_read_b64_tr_b16 v[54:55], v138 offset:26112
	ds_read_b64_tr_b16 v[56:57], v138 offset:26624
	ds_read_b64_tr_b16 v[58:59], v138 offset:27136
	ds_read_b64_tr_b16 v[76:77], v138 offset:27648
	ds_read_b64_tr_b16 v[78:79], v138 offset:28160
	v_mfma_f32_32x32x16_bf16 v[16:31], v[60:63], v[88:91], v[16:31]
	ds_read_b64_tr_b16 v[80:81], v138 offset:28672
	ds_read_b64_tr_b16 v[82:83], v138 offset:29184
	ds_read_b64_tr_b16 v[84:85], v138 offset:29696
	ds_read_b64_tr_b16 v[86:87], v138 offset:30208
	ds_read_b64_tr_b16 v[88:89], v138 offset:30720
	ds_read_b64_tr_b16 v[90:91], v138 offset:31232
	ds_read_b64_tr_b16 v[92:93], v138 offset:31744
	ds_read_b64_tr_b16 v[94:95], v138 offset:32256
	s_waitcnt lgkmcnt(14)
	v_mfma_f32_32x32x16_bf16 v[0:15], v[60:63], v[104:107], v[0:15]
	v_mfma_f32_32x32x16_bf16 v[16:31], v[64:67], v[48:51], v[16:31]
	s_waitcnt lgkmcnt(6)
	v_mfma_f32_32x32x16_bf16 v[0:15], v[64:67], v[80:83], v[0:15]
	v_mfma_f32_32x32x16_bf16 v[16:31], v[68:71], v[52:55], v[16:31]
	s_waitcnt lgkmcnt(4)
	v_mfma_f32_32x32x16_bf16 v[0:15], v[68:71], v[84:87], v[0:15]
	v_mfma_f32_32x32x16_bf16 v[16:31], v[72:75], v[56:59], v[16:31]
	s_waitcnt lgkmcnt(2)
	v_mfma_f32_32x32x16_bf16 v[0:15], v[72:75], v[88:91], v[0:15]
	v_mfma_f32_32x32x16_bf16 v[16:31], v[108:111], v[76:79], v[16:31]
	s_waitcnt lgkmcnt(0)
	v_mfma_f32_32x32x16_bf16 v[0:15], v[108:111], v[92:95], v[0:15]

; #define LAS __attribute__((address_space(3)))
; __device__ __forceinline__ void moba_unit(const MobaArgs& A, int b, int h, int qb, LAS unsigned char* lds, int wave, bool tables) {
;     ...
;         asm volatile("s_waitcnt vmcnt(0)" ::: "memory");
;         __syncthreads();
;         if (j + 1 < NP) { const int j1 = j + 1; const int kt1 = (j1 < 2) ? q0 + 128 * j1 : 256 * (qb - 1 - ((j1 - 2) >> 1)) + 128 * ((j1 - 2) & 1);
;             LAS unsigned char* sl = lds + L_BUF + (j1 & 1) * 32768;
;             stage_tile<64>(sl, Kh + (size_t)kt1 * 512, Vh + (size_t)kt1 * 512, 512, 512, wid, lane);
;             stage_tile<64>(sl + 16384, Kh + (size_t)(kt1 + 64) * 512, Vh + (size_t)(kt1 + 64) * 512, 512, 512, wid, lane); }
.LBB0_726:
	s_waitcnt vmcnt(0)
	s_add_i32 s6, s72, 3
	s_cmp_ge_u32 s6, s76
	s_waitcnt vmcnt(0) lgkmcnt(0)
	s_barrier
	s_cbranch_scc1 .LBB0_730
	s_bitcmp1_b32 s92, 7
	s_cbranch_scc0 .LBB0_730
	s_cmp_eq_u32 s72, -2
	s_mov_b32 s6, s62
	s_cbranch_scc1 .LBB0_729
	s_add_i32 s6, s72, 1
	s_not_b32 s6, s6
	s_lshr_b32 s6, s6, 1
	s_add_i32 s6, s89, s6
	s_add_i32 s7, s73, 0xffffff80
	s_lshl_b32 s6, s6, 8
	s_and_b32 s7, s7, 0x80
	s_or_b32 s6, s6, s7

; __device__ __forceinline__ float fast_rcp(float x) { return __builtin_amdgcn_rcpf(x); }
; __device__ __forceinline__ void moba_unit(const MobaArgs& A, int b, int h, int qb, LAS unsigned char* lds, int wave, bool tables) {
;     ...
;     }
;     ...
;     if (A.stamp != nullptr && tid == 0) { const unsigned long long tot = __builtin_readcyclecounter() - tu0_; *A.stamp = __float_as_uint(20.0f + ((float)tot - 150000.0f) * (1.0f / 500.0f)); }
;     ...
;     const float lt = l + __shfl_xor(l, 32);
;     if (!A.dry) store_o<64>(o, fast_rcp(lt), wsf, ost, A.O + (rowb + q0 + 32 * wid) * 512 + h * HD, 512, lane, r32, hi);
.LBB0_756:
	s_bitcmp1_b32 s92, 7
	s_cbranch_scc1 .Lstg_m2_ex
	s_barrier
